# baseline (speedup 1.0000x reference)
_Z14special_kernelPKtPKfS2_S2_S2_PfS3_S3_S2_S3_:
	s_load_dwordx2 s[16:17], s[0:1], 0x40
	s_load_dwordx4 s[8:11], s[0:1], 0x8
	s_load_dwordx2 s[6:7], s[0:1], 0x18
	v_lshrrev_b32_e32 v1, 8, v0
	v_lshlrev_b32_e32 v22, 6, v1
	s_cmp_lg_u32 s2, 32
	s_mov_b64 s[4:5], -1
	s_cbranch_scc0 .LBB12_12
	s_load_dwordx4 s[12:15], s[0:1], 0x20
	s_load_dwordx2 s[18:19], s[0:1], 0x30
	v_mov_b32_e32 v2, 2
	v_lshlrev_b32_sdwa v2, v2, v0 dst_sel:DWORD dst_unused:UNUSED_PAD src0_sel:DWORD src1_sel:BYTE_0
	v_lshl_or_b32 v16, v1, 16, v2
	v_mov_b32_e32 v3, 0
	v_lshlrev_b32_e32 v24, 8, v1
	v_add_u32_e32 v23, 64, v22
	v_or_b32_e32 v2, 0x3c00, v16
	v_or_b32_e32 v4, 0x3400, v16
	v_mov_b32_e32 v5, v3
	v_or_b32_e32 v25, 0x2000, v24
	v_or_b32_e32 v6, 0x2c00, v16
	v_mov_b32_e32 v7, v3
	v_or_b32_e32 v8, 0x400, v16
	v_mov_b32_e32 v9, v3
	v_or_b32_e32 v10, 0x2400, v16
	v_mov_b32_e32 v11, v3
	v_or_b32_e32 v12, 0x1c00, v16
	v_mov_b32_e32 v13, v3
	v_or_b32_e32 v14, 0xc00, v16
	v_mov_b32_e32 v15, v3
	v_or_b32_e32 v16, 0x1400, v16
	v_mov_b32_e32 v17, v3
	s_mov_b64 s[4:5], 0
	s_waitcnt lgkmcnt(0)
	v_and_b32_e32 v120, 0xff, v0
	v_lshlrev_b32_e32 v120, 2, v120
	v_lshl_or_b32 v121, v1, 11, v120
	v_lshl_or_b32 v55, v1, 16, v120
	v_add_u32_e32 v123, 0x1000, v55
	s_lshl_b32 s28, s2, 13
	s_add_u32 s28, s12, s28
	s_addc_u32 s29, s13, 0
	s_and_b32 s30, s2, 7
	s_lshl_b32 s30, s30, 13
	s_add_u32 s30, s12, s30
	s_addc_u32 s31, s13, 0
	global_load_dword v44, v121, s[28:29]
	global_load_dword v45, v121, s[28:29] offset:1024
	global_load_dword v46, v55, s[30:31]
	global_load_dword v47, v55, s[30:31] offset:1024
	global_load_dword v48, v55, s[30:31] offset:2048
	global_load_dword v49, v55, s[30:31] offset:3072
	global_load_dword v50, v123, s[30:31]
	global_load_dword v51, v123, s[30:31] offset:1024
	global_load_dword v52, v123, s[30:31] offset:2048
	global_load_dword v53, v123, s[30:31] offset:3072
	global_load_dword v54, v120, s[6:7]
	s_mov_b64 s[20:21], s[8:9]
	v_mov_b32_e32 v26, v22
	v_mov_b32_e32 v18, v3
	v_mov_b32_e32 v19, v3
	v_mov_b32_e32 v20, v3
	v_mov_b32_e32 v21, v3
	v_lshl_add_u64 v[28:29], s[20:21], 0, v[8:9]
	v_lshl_add_u64 v[30:31], s[20:21], 0, v[14:15]
	v_lshl_add_u64 v[32:33], s[20:21], 0, v[16:17]
	v_lshl_add_u64 v[34:35], s[20:21], 0, v[12:13]
	v_lshl_add_u64 v[36:37], s[20:21], 0, v[10:11]
	v_lshl_add_u64 v[38:39], s[20:21], 0, v[6:7]
	v_lshl_add_u64 v[40:41], s[20:21], 0, v[4:5]
	v_lshl_add_u64 v[42:43], s[20:21], 0, v[2:3]
	global_load_dword v56, v[28:29], off offset:-1024
	global_load_dword v57, v[28:29], off
	global_load_dword v58, v[30:31], off offset:-1024
	global_load_dword v59, v[30:31], off
	global_load_dword v60, v[32:33], off offset:-1024
	global_load_dword v61, v[32:33], off
	global_load_dword v62, v[34:35], off offset:-1024
	global_load_dword v63, v[34:35], off
	global_load_dword v64, v[36:37], off offset:-1024
	global_load_dword v65, v[36:37], off
	global_load_dword v66, v[38:39], off offset:-1024
	global_load_dword v67, v[38:39], off
	global_load_dword v68, v[40:41], off offset:-1024
	global_load_dword v69, v[40:41], off
	global_load_dword v70, v[42:43], off offset:-1024
	global_load_dword v71, v[42:43], off
	s_add_u32 s20, s20, 0x4000
	s_addc_u32 s21, s21, 0
	v_lshl_add_u64 v[28:29], s[20:21], 0, v[8:9]
	v_lshl_add_u64 v[30:31], s[20:21], 0, v[14:15]
	v_lshl_add_u64 v[32:33], s[20:21], 0, v[16:17]
	v_lshl_add_u64 v[34:35], s[20:21], 0, v[12:13]
	v_lshl_add_u64 v[36:37], s[20:21], 0, v[10:11]
	v_lshl_add_u64 v[38:39], s[20:21], 0, v[6:7]
	v_lshl_add_u64 v[40:41], s[20:21], 0, v[4:5]
	v_lshl_add_u64 v[42:43], s[20:21], 0, v[2:3]
	global_load_dword v72, v[28:29], off offset:-1024
	global_load_dword v73, v[28:29], off
	global_load_dword v74, v[30:31], off offset:-1024
	global_load_dword v75, v[30:31], off
	global_load_dword v76, v[32:33], off offset:-1024
	global_load_dword v77, v[32:33], off
	global_load_dword v78, v[34:35], off offset:-1024
	global_load_dword v79, v[34:35], off
	global_load_dword v80, v[36:37], off offset:-1024
	global_load_dword v81, v[36:37], off
	global_load_dword v82, v[38:39], off offset:-1024
	global_load_dword v83, v[38:39], off
	global_load_dword v84, v[40:41], off offset:-1024
	global_load_dword v85, v[40:41], off
	global_load_dword v86, v[42:43], off offset:-1024
	global_load_dword v87, v[42:43], off
	s_add_u32 s20, s20, 0x4000
	s_addc_u32 s21, s21, 0
	v_lshl_add_u64 v[28:29], s[20:21], 0, v[8:9]
	v_lshl_add_u64 v[30:31], s[20:21], 0, v[14:15]
	v_lshl_add_u64 v[32:33], s[20:21], 0, v[16:17]
	v_lshl_add_u64 v[34:35], s[20:21], 0, v[12:13]
	v_lshl_add_u64 v[36:37], s[20:21], 0, v[10:11]
	v_lshl_add_u64 v[38:39], s[20:21], 0, v[6:7]
	v_lshl_add_u64 v[40:41], s[20:21], 0, v[4:5]
	v_lshl_add_u64 v[42:43], s[20:21], 0, v[2:3]
	global_load_dword v88, v[28:29], off offset:-1024
	global_load_dword v89, v[28:29], off
	global_load_dword v90, v[30:31], off offset:-1024
	global_load_dword v91, v[30:31], off
	global_load_dword v92, v[32:33], off offset:-1024
	global_load_dword v93, v[32:33], off
	global_load_dword v94, v[34:35], off offset:-1024
	global_load_dword v95, v[34:35], off
	global_load_dword v96, v[36:37], off offset:-1024
	global_load_dword v97, v[36:37], off
	global_load_dword v98, v[38:39], off offset:-1024
	global_load_dword v99, v[38:39], off
	global_load_dword v100, v[40:41], off offset:-1024
	global_load_dword v101, v[40:41], off
	global_load_dword v102, v[42:43], off offset:-1024
	global_load_dword v103, v[42:43], off
	s_add_u32 s20, s20, 0x4000
	s_addc_u32 s21, s21, 0
	s_movk_i32 s3, 0x200
	v_cmp_gt_u32_e32 vcc, s3, v0
	s_and_saveexec_b64 s[4:5], vcc
	s_cbranch_execz .LBB12_3
	s_load_dwordx2 s[24:25], s[0:1], 0x0
	s_mul_i32 s26, s2, 0x210
	v_lshrrev_b32_e32 v124, 4, v0
	s_mul_hi_i32 s3, s2, 0x210
	s_add_u32 s26, s26, 0x200
	v_bfe_u32 v125, v0, 4, 1
	s_addc_u32 s3, s3, 0
	v_and_b32_e32 v124, 14, v124
	v_lshrrev_b32_e32 v126, 1, v0
	v_and_b32_e32 v127, 3, v0
	v_or3_b32 v124, s26, v124, v125
	v_mov_b32_e32 v125, s3
	v_and_or_b32 v122, v126, 4, v127
	v_lshlrev_b64 v[124:125], 10, v[124:125]
	v_lshlrev_b32_e32 v126, 7, v0
	s_waitcnt lgkmcnt(0)
	v_lshl_add_u64 v[124:125], s[24:25], 0, v[124:125]
	v_and_b32_e32 v126, 0x200, v126
	v_mov_b32_e32 v127, 0
	v_lshl_add_u64 v[124:125], v[124:125], 0, v[126:127]
	v_lshlrev_b32_e32 v126, 4, v1
	v_lshl_add_u64 v[124:125], v[124:125], 0, v[126:127]
	v_lshlrev_b32_e32 v126, 1, v122
	v_lshl_add_u64 v[124:125], v[124:125], 0, v[126:127]
	global_load_ushort v124, v[124:125], off
	v_mov_b32_e32 v125, 2
	v_lshlrev_b32_sdwa v125, v125, v0 dst_sel:DWORD dst_unused:UNUSED_PAD src0_sel:DWORD src1_sel:BYTE_0
	global_load_dword v126, v125, s[16:17]
	v_lshl_or_b32 v125, v1, 10, v125
	s_waitcnt vmcnt(1)
	v_lshlrev_b32_e32 v124, 16, v124
	s_waitcnt vmcnt(0)
	v_add_f32_e32 v124, v126, v124
	ds_write_b32 v125, v124 offset:8192
.LBB12_3:
	s_or_b64 exec, exec, s[4:5]
	s_waitcnt vmcnt(32)
	v_add_f32_e32 v44, v44, v45
	v_add_f32_e32 v46, v46, v47
	v_add_f32_e32 v48, v48, v49
	v_add_f32_e32 v50, v50, v51
	v_add_f32_e32 v52, v52, v53
	v_add_f32_e32 v46, v46, v48
	v_add_f32_e32 v50, v50, v52
	v_add_f32_e32 v46, v46, v50
	v_cmp_eq_u32_e32 vcc, 0, v1
	s_nop 1
	v_cndmask_b32_e32 v54, 0, v54, vcc
	v_fmamk_f32 v44, v44, 0x3a800000, v54
	v_fmamk_f32 v46, v46, 0x39800000, v54
	v_lshl_or_b32 v45, v1, 10, v120
	ds_write_b32 v45, v44 offset:11264
	ds_write_b32 v45, v46 offset:15360
	v_lshl_add_u64 v[28:29], s[20:21], 0, v[8:9]
	v_lshl_add_u64 v[30:31], s[20:21], 0, v[14:15]
	v_lshl_add_u64 v[32:33], s[20:21], 0, v[16:17]
	v_lshl_add_u64 v[34:35], s[20:21], 0, v[12:13]
	v_lshl_add_u64 v[36:37], s[20:21], 0, v[10:11]
	v_lshl_add_u64 v[38:39], s[20:21], 0, v[6:7]
	v_lshl_add_u64 v[40:41], s[20:21], 0, v[4:5]
	v_lshl_add_u64 v[42:43], s[20:21], 0, v[2:3]
	global_load_dword v104, v[28:29], off offset:-1024
	global_load_dword v105, v[28:29], off
	global_load_dword v106, v[30:31], off offset:-1024
	global_load_dword v107, v[30:31], off
	global_load_dword v108, v[32:33], off offset:-1024
	global_load_dword v109, v[32:33], off
	global_load_dword v110, v[34:35], off offset:-1024
	global_load_dword v111, v[34:35], off
	global_load_dword v112, v[36:37], off offset:-1024
	global_load_dword v113, v[36:37], off
	global_load_dword v114, v[38:39], off offset:-1024
	global_load_dword v115, v[38:39], off
	global_load_dword v116, v[40:41], off offset:-1024
	global_load_dword v117, v[40:41], off
	global_load_dword v118, v[42:43], off offset:-1024
	global_load_dword v119, v[42:43], off
	s_add_u32 s20, s20, 0x4000
	s_addc_u32 s21, s21, 0
	s_waitcnt lgkmcnt(0)
	s_barrier
	ds_read_b128 v[28:31], v25 offset:0
	ds_read_b128 v[32:35], v25 offset:16
	ds_read_b128 v[36:39], v25 offset:32
	ds_read_b128 v[40:43], v25 offset:48
	ds_read_b128 v[44:47], v25 offset:1024
	ds_read_b128 v[48:51], v25 offset:1040
	ds_read_b128 v[52:55], v25 offset:1056
	ds_read_b128 v[120:123], v25 offset:1072
	s_waitcnt vmcnt(48) lgkmcnt(0)
	v_pk_fma_f32 v[20:21], v[56:57], v[28:29], v[20:21]
	v_pk_fma_f32 v[18:19], v[56:57], v[44:45], v[18:19]
	v_pk_fma_f32 v[20:21], v[58:59], v[30:31], v[20:21]
	v_pk_fma_f32 v[18:19], v[58:59], v[46:47], v[18:19]
	v_pk_fma_f32 v[20:21], v[60:61], v[32:33], v[20:21]
	v_pk_fma_f32 v[18:19], v[60:61], v[48:49], v[18:19]
	v_pk_fma_f32 v[20:21], v[62:63], v[34:35], v[20:21]
	v_pk_fma_f32 v[18:19], v[62:63], v[50:51], v[18:19]
	v_pk_fma_f32 v[20:21], v[64:65], v[36:37], v[20:21]
	v_pk_fma_f32 v[18:19], v[64:65], v[52:53], v[18:19]
	v_pk_fma_f32 v[20:21], v[66:67], v[38:39], v[20:21]
	v_pk_fma_f32 v[18:19], v[66:67], v[54:55], v[18:19]
	v_pk_fma_f32 v[20:21], v[68:69], v[40:41], v[20:21]
	v_pk_fma_f32 v[18:19], v[68:69], v[120:121], v[18:19]
	v_pk_fma_f32 v[20:21], v[70:71], v[42:43], v[20:21]
	v_pk_fma_f32 v[18:19], v[70:71], v[122:123], v[18:19]
	ds_read_b128 v[28:31], v25 offset:64
	ds_read_b128 v[32:35], v25 offset:80
	ds_read_b128 v[36:39], v25 offset:96
	ds_read_b128 v[40:43], v25 offset:112
	ds_read_b128 v[44:47], v25 offset:1088
	ds_read_b128 v[48:51], v25 offset:1104
	ds_read_b128 v[52:55], v25 offset:1120
	ds_read_b128 v[120:123], v25 offset:1136
	s_waitcnt vmcnt(32) lgkmcnt(0)
	v_pk_fma_f32 v[20:21], v[72:73], v[28:29], v[20:21]
	v_pk_fma_f32 v[18:19], v[72:73], v[44:45], v[18:19]
	v_pk_fma_f32 v[20:21], v[74:75], v[30:31], v[20:21]
	v_pk_fma_f32 v[18:19], v[74:75], v[46:47], v[18:19]
	v_pk_fma_f32 v[20:21], v[76:77], v[32:33], v[20:21]
	v_pk_fma_f32 v[18:19], v[76:77], v[48:49], v[18:19]
	v_pk_fma_f32 v[20:21], v[78:79], v[34:35], v[20:21]
	v_pk_fma_f32 v[18:19], v[78:79], v[50:51], v[18:19]
	v_pk_fma_f32 v[20:21], v[80:81], v[36:37], v[20:21]
	v_pk_fma_f32 v[18:19], v[80:81], v[52:53], v[18:19]
	v_pk_fma_f32 v[20:21], v[82:83], v[38:39], v[20:21]
	v_pk_fma_f32 v[18:19], v[82:83], v[54:55], v[18:19]
	v_pk_fma_f32 v[20:21], v[84:85], v[40:41], v[20:21]
	v_pk_fma_f32 v[18:19], v[84:85], v[120:121], v[18:19]
	v_pk_fma_f32 v[20:21], v[86:87], v[42:43], v[20:21]
	v_pk_fma_f32 v[18:19], v[86:87], v[122:123], v[18:19]
	ds_read_b128 v[28:31], v25 offset:128
	ds_read_b128 v[32:35], v25 offset:144
	ds_read_b128 v[36:39], v25 offset:160
	ds_read_b128 v[40:43], v25 offset:176
	ds_read_b128 v[44:47], v25 offset:1152
	ds_read_b128 v[48:51], v25 offset:1168
	ds_read_b128 v[52:55], v25 offset:1184
	ds_read_b128 v[120:123], v25 offset:1200
	s_waitcnt vmcnt(16) lgkmcnt(0)
	v_pk_fma_f32 v[20:21], v[88:89], v[28:29], v[20:21]
	v_pk_fma_f32 v[18:19], v[88:89], v[44:45], v[18:19]
	v_pk_fma_f32 v[20:21], v[90:91], v[30:31], v[20:21]
	v_pk_fma_f32 v[18:19], v[90:91], v[46:47], v[18:19]
	v_pk_fma_f32 v[20:21], v[92:93], v[32:33], v[20:21]
	v_pk_fma_f32 v[18:19], v[92:93], v[48:49], v[18:19]
	v_pk_fma_f32 v[20:21], v[94:95], v[34:35], v[20:21]
	v_pk_fma_f32 v[18:19], v[94:95], v[50:51], v[18:19]
	v_pk_fma_f32 v[20:21], v[96:97], v[36:37], v[20:21]
	v_pk_fma_f32 v[18:19], v[96:97], v[52:53], v[18:19]
	v_pk_fma_f32 v[20:21], v[98:99], v[38:39], v[20:21]
	v_pk_fma_f32 v[18:19], v[98:99], v[54:55], v[18:19]
	v_pk_fma_f32 v[20:21], v[100:101], v[40:41], v[20:21]
	v_pk_fma_f32 v[18:19], v[100:101], v[120:121], v[18:19]
	v_pk_fma_f32 v[20:21], v[102:103], v[42:43], v[20:21]
	v_pk_fma_f32 v[18:19], v[102:103], v[122:123], v[18:19]
	ds_read_b128 v[28:31], v25 offset:192
	ds_read_b128 v[32:35], v25 offset:208
	ds_read_b128 v[36:39], v25 offset:224
	ds_read_b128 v[40:43], v25 offset:240
	ds_read_b128 v[44:47], v25 offset:1216
	ds_read_b128 v[48:51], v25 offset:1232
	ds_read_b128 v[52:55], v25 offset:1248
	ds_read_b128 v[120:123], v25 offset:1264
	s_waitcnt vmcnt(0) lgkmcnt(0)
	v_pk_fma_f32 v[20:21], v[104:105], v[28:29], v[20:21]
	v_pk_fma_f32 v[18:19], v[104:105], v[44:45], v[18:19]
	v_pk_fma_f32 v[20:21], v[106:107], v[30:31], v[20:21]
	v_pk_fma_f32 v[18:19], v[106:107], v[46:47], v[18:19]
	v_pk_fma_f32 v[20:21], v[108:109], v[32:33], v[20:21]
	v_pk_fma_f32 v[18:19], v[108:109], v[48:49], v[18:19]
	v_pk_fma_f32 v[20:21], v[110:111], v[34:35], v[20:21]
	v_pk_fma_f32 v[18:19], v[110:111], v[50:51], v[18:19]
	v_pk_fma_f32 v[20:21], v[112:113], v[36:37], v[20:21]
	v_pk_fma_f32 v[18:19], v[112:113], v[52:53], v[18:19]
	v_pk_fma_f32 v[20:21], v[114:115], v[38:39], v[20:21]
	v_pk_fma_f32 v[18:19], v[114:115], v[54:55], v[18:19]
	v_pk_fma_f32 v[20:21], v[116:117], v[40:41], v[20:21]
	v_pk_fma_f32 v[18:19], v[116:117], v[120:121], v[18:19]
	v_pk_fma_f32 v[20:21], v[118:119], v[42:43], v[20:21]
	v_pk_fma_f32 v[18:19], v[118:119], v[122:123], v[18:19]
	s_or_b64 exec, exec, s[4:5]
	v_add_f32_e32 v20, v20, v21
	v_mov_b32_e32 v21, 2
	v_lshlrev_b32_sdwa v26, v21, v0 dst_sel:DWORD dst_unused:UNUSED_PAD src0_sel:DWORD src1_sel:BYTE_0
	v_lshl_or_b32 v25, v1, 10, v26
	v_add_f32_e32 v18, v18, v19
	s_movk_i32 s3, 0x100
	ds_write2st64_b32 v25, v20, v18 offset1:16
	v_cmp_gt_u32_e64 s[4:5], s3, v0
	v_lshl_or_b32 v18, s2, 8, v0
	s_waitcnt lgkmcnt(0)
	s_barrier
	s_mov_b64 s[12:13], s[10:11]
	v_lshl_add_u64 v[122:123], s[12:13], 0, v[8:9]
	v_lshl_add_u64 v[28:29], s[12:13], 0, v[14:15]
	v_lshl_add_u64 v[30:31], s[12:13], 0, v[16:17]
	v_lshl_add_u64 v[32:33], s[12:13], 0, v[12:13]
	v_lshl_add_u64 v[34:35], s[12:13], 0, v[10:11]
	v_lshl_add_u64 v[36:37], s[12:13], 0, v[6:7]
	v_lshl_add_u64 v[38:39], s[12:13], 0, v[4:5]
	v_lshl_add_u64 v[40:41], s[12:13], 0, v[2:3]
	global_load_dword v42, v[122:123], off offset:-1024
	global_load_dword v43, v[122:123], off
	global_load_dword v44, v[28:29], off offset:-1024
	global_load_dword v45, v[28:29], off
	global_load_dword v46, v[30:31], off offset:-1024
	global_load_dword v47, v[30:31], off
	global_load_dword v48, v[32:33], off offset:-1024
	global_load_dword v49, v[32:33], off
	global_load_dword v50, v[34:35], off offset:-1024
	global_load_dword v51, v[34:35], off
	global_load_dword v52, v[36:37], off offset:-1024
	global_load_dword v53, v[36:37], off
	global_load_dword v54, v[38:39], off offset:-1024
	global_load_dword v55, v[38:39], off
	global_load_dword v56, v[40:41], off offset:-1024
	global_load_dword v57, v[40:41], off
	s_add_u32 s12, s12, 0x4000
	s_addc_u32 s13, s13, 0
	v_lshl_add_u64 v[122:123], s[12:13], 0, v[8:9]
	v_lshl_add_u64 v[28:29], s[12:13], 0, v[14:15]
	v_lshl_add_u64 v[30:31], s[12:13], 0, v[16:17]
	v_lshl_add_u64 v[32:33], s[12:13], 0, v[12:13]
	v_lshl_add_u64 v[34:35], s[12:13], 0, v[10:11]
	v_lshl_add_u64 v[36:37], s[12:13], 0, v[6:7]
	v_lshl_add_u64 v[38:39], s[12:13], 0, v[4:5]
	v_lshl_add_u64 v[40:41], s[12:13], 0, v[2:3]
	global_load_dword v72, v[122:123], off offset:-1024
	global_load_dword v73, v[122:123], off
	global_load_dword v74, v[28:29], off offset:-1024
	global_load_dword v75, v[28:29], off
	global_load_dword v76, v[30:31], off offset:-1024
	global_load_dword v77, v[30:31], off
	global_load_dword v78, v[32:33], off offset:-1024
	global_load_dword v79, v[32:33], off
	global_load_dword v80, v[34:35], off offset:-1024
	global_load_dword v81, v[34:35], off
	global_load_dword v82, v[36:37], off offset:-1024
	global_load_dword v83, v[36:37], off
	global_load_dword v84, v[38:39], off offset:-1024
	global_load_dword v85, v[38:39], off
	global_load_dword v86, v[40:41], off offset:-1024
	global_load_dword v87, v[40:41], off
	s_add_u32 s12, s12, 0x4000
	s_addc_u32 s13, s13, 0
	v_lshl_add_u64 v[122:123], s[12:13], 0, v[8:9]
	v_lshl_add_u64 v[28:29], s[12:13], 0, v[14:15]
	v_lshl_add_u64 v[30:31], s[12:13], 0, v[16:17]
	v_lshl_add_u64 v[32:33], s[12:13], 0, v[12:13]
	v_lshl_add_u64 v[34:35], s[12:13], 0, v[10:11]
	v_lshl_add_u64 v[36:37], s[12:13], 0, v[6:7]
	v_lshl_add_u64 v[38:39], s[12:13], 0, v[4:5]
	v_lshl_add_u64 v[40:41], s[12:13], 0, v[2:3]
	global_load_dword v88, v[122:123], off offset:-1024
	global_load_dword v89, v[122:123], off
	global_load_dword v90, v[28:29], off offset:-1024
	global_load_dword v91, v[28:29], off
	global_load_dword v92, v[30:31], off offset:-1024
	global_load_dword v93, v[30:31], off
	global_load_dword v94, v[32:33], off offset:-1024
	global_load_dword v95, v[32:33], off
	global_load_dword v96, v[34:35], off offset:-1024
	global_load_dword v97, v[34:35], off
	global_load_dword v98, v[36:37], off offset:-1024
	global_load_dword v99, v[36:37], off
	global_load_dword v100, v[38:39], off offset:-1024
	global_load_dword v101, v[38:39], off
	global_load_dword v102, v[40:41], off offset:-1024
	global_load_dword v103, v[40:41], off
	s_add_u32 s12, s12, 0x4000
	s_addc_u32 s13, s13, 0
	s_and_saveexec_b64 s[20:21], s[4:5]
	s_cbranch_execz .LBB12_7
	ds_read2st64_b32 v[28:29], v26 offset1:4
	ds_read2st64_b32 v[30:31], v26 offset0:8 offset1:12
	ds_read2st64_b32 v[32:33], v26 offset0:16 offset1:20
	ds_read2st64_b32 v[34:35], v26 offset0:24 offset1:28
	ds_read2st64_b32 v[36:37], v26 offset0:44 offset1:48
	ds_read2st64_b32 v[38:39], v26 offset0:52 offset1:56
	ds_read2st64_b32 v[40:41], v26 offset0:60 offset1:64
	ds_read2st64_b32 v[120:121], v26 offset0:68 offset1:72
	v_ashrrev_i32_e32 v19, 31, v18
	v_lshl_add_u64 v[20:21], v[18:19], 2, s[14:15]
	s_waitcnt lgkmcnt(0)
	v_add_f32_e32 v28, v28, v29
	v_add_f32_e32 v30, v30, v31
	v_add_f32_e32 v36, v36, v37
	v_add_f32_e32 v38, v38, v39
	v_add_f32_e32 v28, v28, v30
	v_add_f32_e32 v36, v36, v38
	v_add_f32_e32 v28, v28, v36
	v_add_f32_e32 v32, v32, v33
	v_add_f32_e32 v34, v34, v35
	v_add_f32_e32 v40, v40, v41
	v_add_f32_e32 v120, v120, v121
	v_add_f32_e32 v32, v32, v34
	v_add_f32_e32 v40, v40, v120
	v_add_f32_e32 v32, v32, v40
	global_store_dword v[20:21], v28, off
	ds_write_b32 v26, v32 offset:10240
.LBB12_7:
	s_or_b64 exec, exec, s[20:21]
	v_mov_b32_e32 v20, 0
	v_or_b32_e32 v19, 0x2800, v24
	s_mov_b64 s[2:3], 0
	v_mov_b32_e32 v24, v22
	v_mov_b32_e32 v21, v20
	s_waitcnt vmcnt(46)
	v_lshl_add_u64 v[122:123], s[12:13], 0, v[8:9]
	v_lshl_add_u64 v[28:29], s[12:13], 0, v[14:15]
	v_lshl_add_u64 v[30:31], s[12:13], 0, v[16:17]
	v_lshl_add_u64 v[32:33], s[12:13], 0, v[12:13]
	v_lshl_add_u64 v[34:35], s[12:13], 0, v[10:11]
	v_lshl_add_u64 v[36:37], s[12:13], 0, v[6:7]
	v_lshl_add_u64 v[38:39], s[12:13], 0, v[4:5]
	v_lshl_add_u64 v[40:41], s[12:13], 0, v[2:3]
	global_load_dword v104, v[122:123], off offset:-1024
	global_load_dword v105, v[122:123], off
	global_load_dword v106, v[28:29], off offset:-1024
	global_load_dword v107, v[28:29], off
	global_load_dword v108, v[30:31], off offset:-1024
	global_load_dword v109, v[30:31], off
	global_load_dword v110, v[32:33], off offset:-1024
	global_load_dword v111, v[32:33], off
	global_load_dword v112, v[34:35], off offset:-1024
	global_load_dword v113, v[34:35], off
	global_load_dword v114, v[36:37], off offset:-1024
	global_load_dword v115, v[36:37], off
	global_load_dword v116, v[38:39], off offset:-1024
	global_load_dword v117, v[38:39], off
	global_load_dword v118, v[40:41], off offset:-1024
	global_load_dword v119, v[40:41], off
	s_add_u32 s12, s12, 0x4000
	s_addc_u32 s13, s13, 0
	s_waitcnt lgkmcnt(0)
	s_barrier
	ds_read_b128 v[26:29], v19 offset:0
	ds_read_b128 v[30:33], v19 offset:16
	ds_read_b128 v[34:37], v19 offset:32
	ds_read_b128 v[38:41], v19 offset:48
	s_waitcnt vmcnt(48) lgkmcnt(0)
	v_pk_fma_f32 v[20:21], v[42:43], v[26:27], v[20:21]
	v_pk_fma_f32 v[20:21], v[44:45], v[28:29], v[20:21]
	v_pk_fma_f32 v[20:21], v[46:47], v[30:31], v[20:21]
	v_pk_fma_f32 v[20:21], v[48:49], v[32:33], v[20:21]
	v_pk_fma_f32 v[20:21], v[50:51], v[34:35], v[20:21]
	v_pk_fma_f32 v[20:21], v[52:53], v[36:37], v[20:21]
	v_pk_fma_f32 v[20:21], v[54:55], v[38:39], v[20:21]
	v_pk_fma_f32 v[20:21], v[56:57], v[40:41], v[20:21]
	ds_read_b128 v[26:29], v19 offset:64
	ds_read_b128 v[30:33], v19 offset:80
	ds_read_b128 v[34:37], v19 offset:96
	ds_read_b128 v[38:41], v19 offset:112
	s_waitcnt vmcnt(32) lgkmcnt(0)
	v_pk_fma_f32 v[20:21], v[72:73], v[26:27], v[20:21]
	v_pk_fma_f32 v[20:21], v[74:75], v[28:29], v[20:21]
	v_pk_fma_f32 v[20:21], v[76:77], v[30:31], v[20:21]
	v_pk_fma_f32 v[20:21], v[78:79], v[32:33], v[20:21]
	v_pk_fma_f32 v[20:21], v[80:81], v[34:35], v[20:21]
	v_pk_fma_f32 v[20:21], v[82:83], v[36:37], v[20:21]
	v_pk_fma_f32 v[20:21], v[84:85], v[38:39], v[20:21]
	v_pk_fma_f32 v[20:21], v[86:87], v[40:41], v[20:21]
	ds_read_b128 v[26:29], v19 offset:128
	ds_read_b128 v[30:33], v19 offset:144
	ds_read_b128 v[34:37], v19 offset:160
	ds_read_b128 v[38:41], v19 offset:176
	s_waitcnt vmcnt(16) lgkmcnt(0)
	v_pk_fma_f32 v[20:21], v[88:89], v[26:27], v[20:21]
	v_pk_fma_f32 v[20:21], v[90:91], v[28:29], v[20:21]
	v_pk_fma_f32 v[20:21], v[92:93], v[30:31], v[20:21]
	v_pk_fma_f32 v[20:21], v[94:95], v[32:33], v[20:21]
	v_pk_fma_f32 v[20:21], v[96:97], v[34:35], v[20:21]
	v_pk_fma_f32 v[20:21], v[98:99], v[36:37], v[20:21]
	v_pk_fma_f32 v[20:21], v[100:101], v[38:39], v[20:21]
	v_pk_fma_f32 v[20:21], v[102:103], v[40:41], v[20:21]
	ds_read_b128 v[26:29], v19 offset:192
	ds_read_b128 v[30:33], v19 offset:208
	ds_read_b128 v[34:37], v19 offset:224
	ds_read_b128 v[38:41], v19 offset:240
	s_waitcnt vmcnt(0) lgkmcnt(0)
	v_pk_fma_f32 v[20:21], v[104:105], v[26:27], v[20:21]
	v_pk_fma_f32 v[20:21], v[106:107], v[28:29], v[20:21]
	v_pk_fma_f32 v[20:21], v[108:109], v[30:31], v[20:21]
	v_pk_fma_f32 v[20:21], v[110:111], v[32:33], v[20:21]
	v_pk_fma_f32 v[20:21], v[112:113], v[34:35], v[20:21]
	v_pk_fma_f32 v[20:21], v[114:115], v[36:37], v[20:21]
	v_pk_fma_f32 v[20:21], v[116:117], v[38:39], v[20:21]
	v_pk_fma_f32 v[20:21], v[118:119], v[40:41], v[20:21]
	s_or_b64 exec, exec, s[2:3]
	v_add_f32_e32 v2, v20, v21
	ds_write_b32 v25, v2
	s_waitcnt lgkmcnt(0)
	s_barrier
	s_and_saveexec_b64 s[2:3], s[4:5]
	s_cbranch_execz .LBB12_11
	v_mov_b32_e32 v2, 2
	v_lshlrev_b32_sdwa v4, v2, v0 dst_sel:DWORD dst_unused:UNUSED_PAD src0_sel:DWORD src1_sel:BYTE_0
	ds_read2st64_b32 v[2:3], v4 offset1:4
	ds_read2st64_b32 v[4:5], v4 offset0:8 offset1:12
	v_ashrrev_i32_e32 v19, 31, v18
	s_waitcnt lgkmcnt(1)
	v_mov_b32_e32 v6, v2
	s_waitcnt lgkmcnt(0)
	v_mov_b32_e32 v7, v4
	v_mov_b32_e32 v4, v3
	v_pk_add_f32 v[2:3], v[6:7], v[4:5]
	s_nop 0
	v_add_f32_e32 v4, v2, v3
	v_lshl_add_u64 v[2:3], v[18:19], 2, s[18:19]
	global_store_dword v[2:3], v4, off

	.amdhsa_kernel _Z14special_kernelPKtPKfS2_S2_S2_PfS3_S3_S2_S3_
		.amdhsa_group_segment_fixed_size 19456
		.amdhsa_private_segment_fixed_size 0
		.amdhsa_kernarg_size 80
		.amdhsa_user_sgpr_count 2
		.amdhsa_user_sgpr_dispatch_ptr 0
		.amdhsa_user_sgpr_queue_ptr 0
		.amdhsa_user_sgpr_kernarg_segment_ptr 1
		.amdhsa_user_sgpr_dispatch_id 0
		.amdhsa_user_sgpr_kernarg_preload_length 0
		.amdhsa_user_sgpr_kernarg_preload_offset 0
		.amdhsa_user_sgpr_private_segment_size 0
		.amdhsa_uses_dynamic_stack 0
		.amdhsa_enable_private_segment 0
		.amdhsa_system_sgpr_workgroup_id_x 1
		.amdhsa_system_sgpr_workgroup_id_y 0
		.amdhsa_system_sgpr_workgroup_id_z 0
		.amdhsa_system_sgpr_workgroup_info 0
		.amdhsa_system_vgpr_workitem_id 0
		.amdhsa_next_free_vgpr 128
		.amdhsa_next_free_sgpr 32
		.amdhsa_accum_offset 128
		.amdhsa_reserve_vcc 1
		.amdhsa_float_round_mode_32 0
		.amdhsa_float_round_mode_16_64 0
		.amdhsa_float_denorm_mode_32 3
		.amdhsa_float_denorm_mode_16_64 3
		.amdhsa_dx10_clamp 1
		.amdhsa_ieee_mode 1
		.amdhsa_fp16_overflow 0
		.amdhsa_tg_split 0
		.amdhsa_exception_fp_ieee_invalid_op 0
		.amdhsa_exception_fp_denorm_src 0
		.amdhsa_exception_fp_ieee_div_zero 0
		.amdhsa_exception_fp_ieee_overflow 0
		.amdhsa_exception_fp_ieee_underflow 0
		.amdhsa_exception_fp_ieee_inexact 0
		.amdhsa_exception_int_div_zero 0
	.end_amdhsa_kernel

amdhsa.kernels:
  - .agpr_count:     0
    .args:
      - .actual_access:  read_only
        .address_space:  global
        .offset:         0
        .size:           8
        .value_kind:     global_buffer
      - .actual_access:  write_only
        .address_space:  global
        .offset:         8
        .size:           8
        .value_kind:     global_buffer
      - .actual_access:  write_only
        .address_space:  global
        .offset:         16
        .size:           8
        .value_kind:     global_buffer
      - .actual_access:  read_only
        .address_space:  global
        .offset:         24
        .size:           8
        .value_kind:     global_buffer
      - .actual_access:  read_only
        .address_space:  global
        .offset:         32
        .size:           8
        .value_kind:     global_buffer
      - .actual_access:  read_only
        .address_space:  global
        .offset:         40
        .size:           8
        .value_kind:     global_buffer
      - .actual_access:  read_only
        .address_space:  global
        .offset:         48
        .size:           8
        .value_kind:     global_buffer
      - .actual_access:  read_only
        .address_space:  global
        .offset:         56
        .size:           8
        .value_kind:     global_buffer
      - .actual_access:  read_only
        .address_space:  global
        .offset:         64
        .size:           8
        .value_kind:     global_buffer
      - .actual_access:  read_only
        .address_space:  global
        .offset:         72
        .size:           8
        .value_kind:     global_buffer
      - .actual_access:  read_only
        .address_space:  global
        .offset:         80
        .size:           8
        .value_kind:     global_buffer
      - .actual_access:  write_only
        .address_space:  global
        .offset:         88
        .size:           8
        .value_kind:     global_buffer
      - .actual_access:  write_only
        .address_space:  global
        .offset:         96
        .size:           8
        .value_kind:     global_buffer
      - .actual_access:  write_only
        .address_space:  global
        .offset:         104
        .size:           8
        .value_kind:     global_buffer
      - .actual_access:  write_only
        .address_space:  global
        .offset:         112
        .size:           8
        .value_kind:     global_buffer
      - .actual_access:  write_only
        .address_space:  global
        .offset:         120
        .size:           8
        .value_kind:     global_buffer
      - .actual_access:  write_only
        .address_space:  global
        .offset:         128
        .size:           8
        .value_kind:     global_buffer
      - .actual_access:  read_only
        .address_space:  global
        .offset:         136
        .size:           8
        .value_kind:     global_buffer
      - .actual_access:  read_only
        .address_space:  global
        .offset:         144
        .size:           8
        .value_kind:     global_buffer
    .group_segment_fixed_size: 0
    .kernarg_segment_align: 8
    .kernarg_segment_size: 152
    .language:       OpenCL C
    .language_version:
      - 2
      - 0
    .max_flat_workgroup_size: 256
    .name:           _Z11prep_kernelPKfPtPfS0_S0_S0_S0_S0_S0_S0_S0_S1_S1_S2_S2_S2_S1_S0_S2_
    .private_segment_fixed_size: 0
    .sgpr_count:     45
    .sgpr_spill_count: 0
    .symbol:         _Z11prep_kernelPKfPtPfS0_S0_S0_S0_S0_S0_S0_S0_S1_S1_S2_S2_S2_S1_S0_S2_.kd
    .uniform_work_group_size: 1
    .uses_dynamic_stack: false
    .vgpr_count:     53
    .vgpr_spill_count: 0
    .wavefront_size: 64
  - .agpr_count:     0
    .args:
      - .actual_access:  read_only
        .address_space:  global
        .offset:         0
        .size:           8
        .value_kind:     global_buffer
      - .actual_access:  write_only
        .address_space:  global
        .offset:         8
        .size:           8
        .value_kind:     global_buffer
      - .actual_access:  write_only
        .address_space:  global
        .offset:         16
        .size:           8
        .value_kind:     global_buffer
      - .offset:         24
        .size:           4
        .value_kind:     hidden_block_count_x
      - .offset:         28
        .size:           4
        .value_kind:     hidden_block_count_y
      - .offset:         32
        .size:           4
        .value_kind:     hidden_block_count_z
      - .offset:         36
        .size:           2
        .value_kind:     hidden_group_size_x
      - .offset:         38
        .size:           2
        .value_kind:     hidden_group_size_y
      - .offset:         40
        .size:           2
        .value_kind:     hidden_group_size_z
      - .offset:         42
        .size:           2
        .value_kind:     hidden_remainder_x
      - .offset:         44
        .size:           2
        .value_kind:     hidden_remainder_y
      - .offset:         46
        .size:           2
        .value_kind:     hidden_remainder_z
      - .offset:         64
        .size:           8
        .value_kind:     hidden_global_offset_x
      - .offset:         72
        .size:           8
        .value_kind:     hidden_global_offset_y
      - .offset:         80
        .size:           8
        .value_kind:     hidden_global_offset_z
      - .offset:         88
        .size:           2
        .value_kind:     hidden_grid_dims
    .group_segment_fixed_size: 0
    .kernarg_segment_align: 8
    .kernarg_segment_size: 280
    .language:       OpenCL C
    .language_version:
      - 2
      - 0
    .max_flat_workgroup_size: 256
    .name:           _Z12prep2_kernelPKfPtPf
    .private_segment_fixed_size: 0
    .sgpr_count:     26
    .sgpr_spill_count: 0
    .symbol:         _Z12prep2_kernelPKfPtPf.kd
    .uniform_work_group_size: 1
    .uses_dynamic_stack: false
    .vgpr_count:     56
    .vgpr_spill_count: 0
    .wavefront_size: 64
  - .agpr_count:     0
    .args:
      - .actual_access:  read_only
        .address_space:  global
        .offset:         0
        .size:           8
        .value_kind:     global_buffer
      - .actual_access:  read_only
        .address_space:  global
        .offset:         8
        .size:           8
        .value_kind:     global_buffer
      - .actual_access:  read_only
        .address_space:  global
        .offset:         16
        .size:           8
        .value_kind:     global_buffer
      - .actual_access:  write_only
        .address_space:  global
        .offset:         24
        .size:           8
        .value_kind:     global_buffer
      - .actual_access:  write_only
        .address_space:  global
        .offset:         32
        .size:           8
        .value_kind:     global_buffer
      - .actual_access:  write_only
        .address_space:  global
        .offset:         40
        .size:           8
        .value_kind:     global_buffer
    .group_segment_fixed_size: 0
    .kernarg_segment_align: 8
    .kernarg_segment_size: 48
    .language:       OpenCL C
    .language_version:
      - 2
      - 0
    .max_flat_workgroup_size: 256
    .name:           _Z9qkv_naivePKtS0_PKfPtS3_S3_
    .private_segment_fixed_size: 0
    .sgpr_count:     22
    .sgpr_spill_count: 0
    .symbol:         _Z9qkv_naivePKtS0_PKfPtS3_S3_.kd
    .uniform_work_group_size: 1
    .uses_dynamic_stack: false
    .vgpr_count:     25
    .vgpr_spill_count: 0
    .wavefront_size: 64
  - .agpr_count:     64
    .args:
      - .actual_access:  read_only
        .address_space:  global
        .offset:         0
        .size:           8
        .value_kind:     global_buffer
      - .actual_access:  read_only
        .address_space:  global
        .offset:         8
        .size:           8
        .value_kind:     global_buffer
      - .actual_access:  read_only
        .address_space:  global
        .offset:         16
        .size:           8
        .value_kind:     global_buffer
      - .actual_access:  write_only
        .address_space:  global
        .offset:         24
        .size:           8
        .value_kind:     global_buffer
      - .actual_access:  write_only
        .address_space:  global
        .offset:         32
        .size:           8
        .value_kind:     global_buffer
      - .actual_access:  write_only
        .address_space:  global
        .offset:         40
        .size:           8
        .value_kind:     global_buffer
    .group_segment_fixed_size: 36864
    .kernarg_segment_align: 8
    .kernarg_segment_size: 48
    .language:       OpenCL C
    .language_version:
      - 2
      - 0
    .max_flat_workgroup_size: 256
    .name:           _Z8qkv_mfmaPKtS0_PKfPtS3_S3_
    .private_segment_fixed_size: 0
    .sgpr_count:     24
    .sgpr_spill_count: 0
    .symbol:         _Z8qkv_mfmaPKtS0_PKfPtS3_S3_.kd
    .uniform_work_group_size: 1
    .uses_dynamic_stack: false
    .vgpr_count:     164
    .vgpr_spill_count: 0
    .wavefront_size: 64
  - .agpr_count:     0
    .args:
      - .actual_access:  read_only
        .address_space:  global
        .offset:         0
        .size:           8
        .value_kind:     global_buffer
      - .address_space:  global
        .offset:         8
        .size:           8
        .value_kind:     global_buffer
      - .actual_access:  read_only
        .address_space:  global
        .offset:         16
        .size:           8
        .value_kind:     global_buffer
      - .actual_access:  write_only
        .address_space:  global
        .offset:         24
        .size:           8
        .value_kind:     global_buffer
      - .actual_access:  write_only
        .address_space:  global
        .offset:         32
        .size:           8
        .value_kind:     global_buffer
      - .actual_access:  write_only
        .address_space:  global
        .offset:         40
        .size:           8
        .value_kind:     global_buffer
    .group_segment_fixed_size: 66048
    .kernarg_segment_align: 8
    .kernarg_segment_size: 48
    .language:       OpenCL C
    .language_version:
      - 2
      - 0
    .max_flat_workgroup_size: 256
    .name:           _Z10qkv_streamPKtS0_PKfPtS3_S3_
    .private_segment_fixed_size: 0
    .sgpr_count:     22
    .sgpr_spill_count: 0
    .symbol:         _Z10qkv_streamPKtS0_PKfPtS3_S3_.kd
    .uniform_work_group_size: 1
    .uses_dynamic_stack: false
    .vgpr_count:     230
    .vgpr_spill_count: 0
    .wavefront_size: 64
  - .agpr_count:     0
    .args:
      - .actual_access:  read_only
        .address_space:  global
        .offset:         0
        .size:           8
        .value_kind:     global_buffer
      - .actual_access:  read_only
        .address_space:  global
        .offset:         8
        .size:           8
        .value_kind:     global_buffer
      - .actual_access:  read_only
        .address_space:  global
        .offset:         16
        .size:           8
        .value_kind:     global_buffer
      - .actual_access:  write_only
        .address_space:  global
        .offset:         24
        .size:           8
        .value_kind:     global_buffer
    .group_segment_fixed_size: 0
    .kernarg_segment_align: 8
    .kernarg_segment_size: 32
    .language:       OpenCL C
    .language_version:
      - 2
      - 0
    .max_flat_workgroup_size: 256
    .name:           _Z10attn_naivePKtS0_S0_Pt
    .private_segment_fixed_size: 0
    .sgpr_count:     20
    .sgpr_spill_count: 0
    .symbol:         _Z10attn_naivePKtS0_S0_Pt.kd
    .uniform_work_group_size: 1
    .uses_dynamic_stack: false
    .vgpr_count:     108
    .vgpr_spill_count: 0
    .wavefront_size: 64
  - .agpr_count:     0
    .args:
      - .actual_access:  read_only
        .address_space:  global
        .offset:         0
        .size:           8
        .value_kind:     global_buffer
      - .address_space:  global
        .offset:         8
        .size:           8
        .value_kind:     global_buffer
      - .actual_access:  read_only
        .address_space:  global
        .offset:         16
        .size:           8
        .value_kind:     global_buffer
      - .actual_access:  read_only
        .address_space:  global
        .offset:         24
        .size:           8
        .value_kind:     global_buffer
      - .address_space:  global
        .offset:         32
        .size:           8
        .value_kind:     global_buffer
      - .actual_access:  write_only
        .address_space:  global
        .offset:         40
        .size:           8
        .value_kind:     global_buffer
      - .actual_access:  write_only
        .address_space:  global
        .offset:         48
        .size:           8
        .value_kind:     global_buffer
    .group_segment_fixed_size: 155648
    .kernarg_segment_align: 8
    .kernarg_segment_size: 56
    .language:       OpenCL C
    .language_version:
      - 2
      - 0
    .max_flat_workgroup_size: 512
    .name:           _Z9attn_mfmaPKtS0_PKfS2_PtS3_S3_
    .private_segment_fixed_size: 0
    .sgpr_count:     41
    .sgpr_spill_count: 0
    .symbol:         _Z9attn_mfmaPKtS0_PKfS2_PtS3_S3_.kd
    .uniform_work_group_size: 1
    .uses_dynamic_stack: false
    .vgpr_count:     215
    .vgpr_spill_count: 0
    .wavefront_size: 64
  - .agpr_count:     0
    .args:
      - .actual_access:  read_only
        .address_space:  global
        .offset:         0
        .size:           8
        .value_kind:     global_buffer
      - .actual_access:  read_only
        .address_space:  global
        .offset:         8
        .size:           8
        .value_kind:     global_buffer
      - .actual_access:  read_only
        .address_space:  global
        .offset:         16
        .size:           8
        .value_kind:     global_buffer
      - .actual_access:  read_only
        .address_space:  global
        .offset:         24
        .size:           8
        .value_kind:     global_buffer
      - .actual_access:  write_only
        .address_space:  global
        .offset:         32
        .size:           8
        .value_kind:     global_buffer
      - .actual_access:  write_only
        .address_space:  global
        .offset:         40
        .size:           8
        .value_kind:     global_buffer
    .group_segment_fixed_size: 0
    .kernarg_segment_align: 8
    .kernarg_segment_size: 48
    .language:       OpenCL C
    .language_version:
      - 2
      - 0
    .max_flat_workgroup_size: 256
    .name:           _Z11special_outPKtS0_PKfS2_PfS3_
    .private_segment_fixed_size: 0
    .sgpr_count:     28
    .sgpr_spill_count: 0
    .symbol:         _Z11special_outPKtS0_PKfS2_PfS3_.kd
    .uniform_work_group_size: 1
    .uses_dynamic_stack: false
    .vgpr_count:     15
    .vgpr_spill_count: 0
    .wavefront_size: 64
  - .agpr_count:     0
    .args:
      - .actual_access:  read_only
        .address_space:  global
        .offset:         0
        .size:           8
        .value_kind:     global_buffer
      - .actual_access:  read_only
        .address_space:  global
        .offset:         8
        .size:           8
        .value_kind:     global_buffer
      - .actual_access:  write_only
        .address_space:  global
        .offset:         16
        .size:           8
        .value_kind:     global_buffer
      - .actual_access:  write_only
        .address_space:  global
        .offset:         24
        .size:           8
        .value_kind:     global_buffer
    .group_segment_fixed_size: 0
    .kernarg_segment_align: 8
    .kernarg_segment_size: 32
    .language:       OpenCL C
    .language_version:
      - 2
      - 0
    .max_flat_workgroup_size: 256
    .name:           _Z6gbuildPKfS0_PfS1_
    .private_segment_fixed_size: 0
    .sgpr_count:     16
    .sgpr_spill_count: 0
    .symbol:         _Z6gbuildPKfS0_PfS1_.kd
    .uniform_work_group_size: 1
    .uses_dynamic_stack: false
    .vgpr_count:     28
    .vgpr_spill_count: 0
    .wavefront_size: 64
  - .agpr_count:     0
    .args:
      - .actual_access:  read_only
        .address_space:  global
        .offset:         0
        .size:           8
        .value_kind:     global_buffer
      - .actual_access:  read_only
        .address_space:  global
        .offset:         8
        .size:           8
        .value_kind:     global_buffer
      - .actual_access:  read_only
        .address_space:  global
        .offset:         16
        .size:           8
        .value_kind:     global_buffer
      - .actual_access:  read_only
        .address_space:  global
        .offset:         24
        .size:           8
        .value_kind:     global_buffer
      - .actual_access:  read_only
        .address_space:  global
        .offset:         32
        .size:           8
        .value_kind:     global_buffer
      - .actual_access:  read_only
        .address_space:  global
        .offset:         40
        .size:           8
        .value_kind:     global_buffer
      - .actual_access:  read_only
        .address_space:  global
        .offset:         48
        .size:           8
        .value_kind:     global_buffer
      - .actual_access:  read_only
        .address_space:  global
        .offset:         56
        .size:           8
        .value_kind:     global_buffer
      - .actual_access:  read_only
        .address_space:  global
        .offset:         64
        .size:           8
        .value_kind:     global_buffer
      - .actual_access:  write_only
        .address_space:  global
        .offset:         72
        .size:           8
        .value_kind:     global_buffer
    .group_segment_fixed_size: 0
    .kernarg_segment_align: 8
    .kernarg_segment_size: 80
    .language:       OpenCL C
    .language_version:
      - 2
      - 0
    .max_flat_workgroup_size: 256
    .name:           _Z13outproj_naivePKtS0_PKfS2_S2_S2_S2_S2_S2_Pf
    .private_segment_fixed_size: 0
    .sgpr_count:     37
    .sgpr_spill_count: 0
    .symbol:         _Z13outproj_naivePKtS0_PKfS2_S2_S2_S2_S2_S2_Pf.kd
    .uniform_work_group_size: 1
    .uses_dynamic_stack: false
    .vgpr_count:     20
    .vgpr_spill_count: 0
    .wavefront_size: 64
  - .agpr_count:     128
    .args:
      - .actual_access:  read_only
        .address_space:  global
        .offset:         0
        .size:           8
        .value_kind:     global_buffer
      - .actual_access:  read_only
        .address_space:  global
        .offset:         8
        .size:           8
        .value_kind:     global_buffer
      - .actual_access:  read_only
        .address_space:  global
        .offset:         16
        .size:           8
        .value_kind:     global_buffer
      - .actual_access:  read_only
        .address_space:  global
        .offset:         24
        .size:           8
        .value_kind:     global_buffer
      - .actual_access:  read_only
        .address_space:  global
        .offset:         32
        .size:           8
        .value_kind:     global_buffer
      - .actual_access:  read_only
        .address_space:  global
        .offset:         40
        .size:           8
        .value_kind:     global_buffer
      - .actual_access:  read_only
        .address_space:  global
        .offset:         48
        .size:           8
        .value_kind:     global_buffer
      - .actual_access:  read_only
        .address_space:  global
        .offset:         56
        .size:           8
        .value_kind:     global_buffer
      - .actual_access:  read_only
        .address_space:  global
        .offset:         64
        .size:           8
        .value_kind:     global_buffer
      - .actual_access:  write_only
        .address_space:  global
        .offset:         72
        .size:           8
        .value_kind:     global_buffer
    .group_segment_fixed_size: 0
    .kernarg_segment_align: 8
    .kernarg_segment_size: 80
    .language:       OpenCL C
    .language_version:
      - 2
      - 0
    .max_flat_workgroup_size: 256
    .name:           _Z12outproj_mfmaPKtS0_PKfS2_S2_S2_S2_S2_S2_Pf
    .private_segment_fixed_size: 0
    .sgpr_count:     30
    .sgpr_spill_count: 0
    .symbol:         _Z12outproj_mfmaPKtS0_PKfS2_S2_S2_S2_S2_S2_Pf.kd
    .uniform_work_group_size: 1
    .uses_dynamic_stack: false
    .vgpr_count:     384
    .vgpr_spill_count: 0
    .wavefront_size: 64
  - .agpr_count:     28
    .args:
      - .address_space:  global
        .offset:         0
        .size:           8
        .value_kind:     global_buffer
      - .actual_access:  read_only
        .address_space:  global
        .offset:         8
        .size:           8
        .value_kind:     global_buffer
      - .actual_access:  read_only
        .address_space:  global
        .offset:         16
        .size:           8
        .value_kind:     global_buffer
      - .actual_access:  read_only
        .address_space:  global
        .offset:         24
        .size:           8
        .value_kind:     global_buffer
      - .actual_access:  read_only
        .address_space:  global
        .offset:         32
        .size:           8
        .value_kind:     global_buffer
      - .actual_access:  read_only
        .address_space:  global
        .offset:         40
        .size:           8
        .value_kind:     global_buffer
    .group_segment_fixed_size: 5632
    .kernarg_segment_align: 8
    .kernarg_segment_size: 48
    .language:       OpenCL C
    .language_version:
      - 2
      - 0
    .max_flat_workgroup_size: 256
    .name:           _Z12gattn_kernelPfPKfS1_S1_S1_S1_
    .private_segment_fixed_size: 0
    .sgpr_count:     98
    .sgpr_spill_count: 0
    .symbol:         _Z12gattn_kernelPfPKfS1_S1_S1_S1_.kd
    .uniform_work_group_size: 1
    .uses_dynamic_stack: false
    .vgpr_count:     284
    .vgpr_spill_count: 0
    .wavefront_size: 64
  - .agpr_count:     0
    .args:
      - .actual_access:  read_only
        .address_space:  global
        .offset:         0
        .size:           8
        .value_kind:     global_buffer
      - .actual_access:  read_only
        .address_space:  global
        .offset:         8
        .size:           8
        .value_kind:     global_buffer
      - .actual_access:  read_only
        .address_space:  global
        .offset:         16
        .size:           8
        .value_kind:     global_buffer
      - .actual_access:  read_only
        .address_space:  global
        .offset:         24
        .size:           8
        .value_kind:     global_buffer
      - .actual_access:  read_only
        .address_space:  global
        .offset:         32
        .size:           8
        .value_kind:     global_buffer
      - .actual_access:  write_only
        .address_space:  global
        .offset:         40
        .size:           8
        .value_kind:     global_buffer
      - .actual_access:  write_only
        .address_space:  global
        .offset:         48
        .size:           8
        .value_kind:     global_buffer
      - .actual_access:  write_only
        .address_space:  global
        .offset:         56
        .size:           8
        .value_kind:     global_buffer
      - .actual_access:  read_only
        .address_space:  global
        .offset:         64
        .size:           8
        .value_kind:     global_buffer
      - .actual_access:  write_only
        .address_space:  global
        .offset:         72
        .size:           8
        .value_kind:     global_buffer
    .group_segment_fixed_size: 19456
    .kernarg_segment_align: 8
    .kernarg_segment_size: 80
    .language:       OpenCL C
    .language_version:
      - 2
      - 0
    .max_flat_workgroup_size: 1024
    .name:           _Z14special_kernelPKtPKfS2_S2_S2_PfS3_S3_S2_S3_
    .private_segment_fixed_size: 0
    .sgpr_count:     33
    .sgpr_spill_count: 0
    .symbol:         _Z14special_kernelPKtPKfS2_S2_S2_PfS3_S3_S2_S3_.kd
    .uniform_work_group_size: 1
    .uses_dynamic_stack: false
    .vgpr_count:     72
    .vgpr_spill_count: 0
    .wavefront_size: 64
  - .agpr_count:     0
    .args:
      - .actual_access:  read_only
        .address_space:  global
        .offset:         0
        .size:           8
        .value_kind:     global_buffer
      - .actual_access:  read_only
        .address_space:  global
        .offset:         8
        .size:           8
        .value_kind:     global_buffer
      - .actual_access:  read_only
        .address_space:  global
        .offset:         16
        .size:           8
        .value_kind:     global_buffer
      - .actual_access:  read_only
        .address_space:  global
        .offset:         24
        .size:           8
        .value_kind:     global_buffer
      - .actual_access:  read_only
        .address_space:  global
        .offset:         32
        .size:           8
        .value_kind:     global_buffer
      - .actual_access:  read_only
        .address_space:  global
        .offset:         40
        .size:           8
        .value_kind:     global_buffer
      - .actual_access:  read_only
        .address_space:  global
        .offset:         48
        .size:           8
        .value_kind:     global_buffer
      - .actual_access:  read_only
        .address_space:  global
        .offset:         56
        .size:           8
        .value_kind:     global_buffer
      - .actual_access:  read_only
        .address_space:  global
        .offset:         64
        .size:           8
        .value_kind:     global_buffer
      - .actual_access:  read_only
        .address_space:  global
        .offset:         72
        .size:           8
        .value_kind:     global_buffer
      - .actual_access:  read_only
        .address_space:  global
        .offset:         80
        .size:           8
        .value_kind:     global_buffer
      - .actual_access:  read_only
        .address_space:  global
        .offset:         88
        .size:           8
        .value_kind:     global_buffer
      - .actual_access:  read_only
        .address_space:  global
        .offset:         96
        .size:           8
        .value_kind:     global_buffer
      - .actual_access:  read_only
        .address_space:  global
        .offset:         104
        .size:           8
        .value_kind:     global_buffer
      - .actual_access:  write_only
        .address_space:  global
        .offset:         112
        .size:           8
        .value_kind:     global_buffer
      - .actual_access:  read_only
        .address_space:  global
        .offset:         120
        .size:           8
        .value_kind:     global_buffer
      - .address_space:  global
        .offset:         128
        .size:           8
        .value_kind:     global_buffer
    .group_segment_fixed_size: 74240
    .kernarg_segment_align: 8
    .kernarg_segment_size: 136
    .language:       OpenCL C
    .language_version:
      - 2
      - 0
    .max_flat_workgroup_size: 512
    .name:           _Z12final_kernelPKtS0_PKfS2_S2_S2_S2_S2_S2_S2_S2_S2_S2_S2_PfPKhS5_
    .private_segment_fixed_size: 0
    .sgpr_count:     34
    .sgpr_spill_count: 0
    .symbol:         _Z12final_kernelPKtS0_PKfS2_S2_S2_S2_S2_S2_S2_S2_S2_S2_S2_PfPKhS5_.kd
    .uniform_work_group_size: 1
    .uses_dynamic_stack: false
    .vgpr_count:     127
    .vgpr_spill_count: 0
    .wavefront_size: 64
